# speedup vs baseline: 1.0093x; 1.0007x over previous
_Z8k_expertPKDF16_S0_PKfPcPiS0_S2_S2_S2_S2_PfS5_S4_S2_S2_S2_S2_S5_S2_S2_S2_:
	s_lshl_b32 s3, s2, 2
	s_load_dwordx8 s[8:15], s[0:1], 0x88
	s_load_dwordx2 s[70:71], s[0:1], 0x0
	s_and_b32 s3, s3, 28
	s_ashr_i32 s4, s2, 6
	s_add_i32 s34, s3, s4
	s_ashr_i32 s6, s34, 1
	v_mov_b32_e32 v2, v0
	s_lshl_b32 s4, s6, 4
	s_ashr_i32 s5, s4, 31
	v_ashrrev_i32_e32 v3, 31, v2
	s_waitcnt lgkmcnt(0)
	v_lshl_add_u64 v[4:5], v[2:3], 2, s[10:11]
	s_lshl_b64 s[10:11], s[4:5], 11
	v_lshl_add_u64 v[6:7], v[4:5], 0, s[10:11]
	s_or_b32 s10, s4, 1
	s_ashr_i32 s11, s10, 31
	s_lshl_b64 s[10:11], s[10:11], 11
	v_lshl_add_u64 v[8:9], v[4:5], 0, s[10:11]
	s_or_b32 s10, s4, 2
	s_ashr_i32 s11, s10, 31
	s_lshl_b64 s[10:11], s[10:11], 11
	v_lshl_add_u64 v[10:11], v[4:5], 0, s[10:11]
	s_or_b32 s10, s4, 3
	s_ashr_i32 s11, s10, 31
	s_lshl_b64 s[10:11], s[10:11], 11
	v_lshl_add_u64 v[12:13], v[4:5], 0, s[10:11]
	s_or_b32 s10, s4, 4
	s_ashr_i32 s11, s10, 31
	s_lshl_b64 s[10:11], s[10:11], 11
	v_lshl_add_u64 v[14:15], v[4:5], 0, s[10:11]
	s_or_b32 s10, s4, 5
	s_ashr_i32 s11, s10, 31
	s_lshl_b64 s[10:11], s[10:11], 11
	v_lshl_add_u64 v[16:17], v[4:5], 0, s[10:11]
	s_or_b32 s10, s4, 6
	s_ashr_i32 s11, s10, 31
	s_lshl_b64 s[10:11], s[10:11], 11
	v_lshl_add_u64 v[18:19], v[4:5], 0, s[10:11]
	s_or_b32 s10, s4, 7
	s_ashr_i32 s11, s10, 31
	s_lshl_b64 s[10:11], s[10:11], 11
	v_lshl_add_u64 v[20:21], v[4:5], 0, s[10:11]
	s_or_b32 s10, s4, 8
	s_ashr_i32 s11, s10, 31
	s_lshl_b64 s[10:11], s[10:11], 11
	global_load_dword v1, v[6:7], off
	global_load_dword v3, v[8:9], off
	global_load_dword v22, v[10:11], off
	global_load_dword v23, v[12:13], off
	global_load_dword v24, v[14:15], off
	global_load_dword v25, v[16:17], off
	global_load_dword v26, v[18:19], off
	global_load_dword v27, v[20:21], off
	v_lshl_add_u64 v[6:7], v[4:5], 0, s[10:11]
	s_or_b32 s10, s4, 9
	s_ashr_i32 s11, s10, 31
	s_lshl_b64 s[10:11], s[10:11], 11
	v_lshl_add_u64 v[8:9], v[4:5], 0, s[10:11]
	s_or_b32 s10, s4, 10
	s_ashr_i32 s11, s10, 31
	s_lshl_b64 s[10:11], s[10:11], 11
	v_lshl_add_u64 v[10:11], v[4:5], 0, s[10:11]
	s_or_b32 s10, s4, 11
	s_ashr_i32 s11, s10, 31
	s_lshl_b64 s[10:11], s[10:11], 11
	v_lshl_add_u64 v[12:13], v[4:5], 0, s[10:11]
	s_or_b32 s10, s4, 12
	s_ashr_i32 s11, s10, 31
	s_lshl_b64 s[10:11], s[10:11], 11
	v_lshl_add_u64 v[14:15], v[4:5], 0, s[10:11]
	s_or_b32 s10, s4, 13
	s_ashr_i32 s11, s10, 31
	s_lshl_b64 s[10:11], s[10:11], 11
	v_lshl_add_u64 v[16:17], v[4:5], 0, s[10:11]
	s_or_b32 s10, s4, 14
	s_or_b32 s4, s4, 15
	s_ashr_i32 s11, s10, 31
	s_ashr_i32 s5, s4, 31
	s_lshl_b64 s[10:11], s[10:11], 11
	s_lshl_b64 s[4:5], s[4:5], 11
	v_lshl_add_u64 v[18:19], v[4:5], 0, s[10:11]
	v_lshl_add_u64 v[4:5], v[4:5], 0, s[4:5]
	global_load_dword v20, v[6:7], off
	global_load_dword v21, v[8:9], off
	global_load_dword v28, v[10:11], off
	global_load_dword v29, v[12:13], off
	global_load_dword v30, v[14:15], off
	global_load_dword v31, v[16:17], off
	global_load_dword v32, v[18:19], off
	global_load_dword v33, v[4:5], off
	v_lshlrev_b32_e32 v4, 3, v2
	v_ashrrev_i32_e32 v5, 31, v4
	v_lshl_add_u64 v[12:13], v[4:5], 2, s[12:13]
	global_load_dwordx4 v[4:7], v[12:13], off
	global_load_dwordx4 v[8:11], v[12:13], off offset:16
	v_and_b32_e32 v200, 63, v0
	v_lshrrev_b32_e32 v201, 6, v0
	v_lshlrev_b32_e32 v202, 4, v200
	v_and_b32_e32 v203, 32, v200
	v_xor_b32_e32 v202, v202, v203
	v_lshrrev_b32_e32 v203, 6, v202
	v_lshrrev_b32_e32 v204, 1, v201
	v_lshl_add_u32 v203, v204, 4, v203
	v_and_b32_e32 v204, 62, v202
	v_and_b32_e32 v205, 1, v201
	v_lshl_add_u32 v204, v205, 6, v204
	v_lshl_add_u32 v200, v203, 12, v204
	v_add_u32_e32 v201, 0x40000, v200
	s_lshl_b32 s72, s6, 22
	s_lshr_b32 s73, s2, 4
	s_and_b32 s73, s73, 3
	s_lshl_b32 s73, s73, 20
	s_add_u32 s72, s72, s73
	s_add_u32 s74, s70, s72
	s_addc_u32 s75, s71, 0
	s_add_u32 s76, s74, 0x80000
	s_addc_u32 s77, s75, 0
	v_readfirstlane_b32 s78, v0
	s_lshl_b32 s78, s78, 4
	s_mov_b32 m0, s78
	s_add_i32 s79, s78, 0x2000
	global_load_lds_dwordx4 v200, s[74:75]
	s_mov_b32 m0, s79
	s_add_i32 s79, s78, 0x4000
	global_load_lds_dwordx4 v201, s[74:75]
	s_mov_b32 m0, s79
	s_add_i32 s79, s78, 0x6000
	global_load_lds_dwordx4 v200, s[76:77]
	s_mov_b32 m0, s79
	s_nop 0
	global_load_lds_dwordx4 v201, s[76:77]
	s_waitcnt vmcnt(21)
	v_add_f32_e32 v1, 0, v1
	s_waitcnt vmcnt(20)
	v_add_f32_e32 v1, v1, v3
	s_waitcnt vmcnt(19)
	v_add_f32_e32 v1, v1, v22
	s_waitcnt vmcnt(18)
	v_add_f32_e32 v1, v1, v23
	s_waitcnt vmcnt(17)
	v_add_f32_e32 v1, v1, v24
	s_waitcnt vmcnt(16)
	v_add_f32_e32 v1, v1, v25
	s_waitcnt vmcnt(15)
	v_add_f32_e32 v1, v1, v26
	s_waitcnt vmcnt(14)
	v_add_f32_e32 v1, v1, v27
	s_waitcnt vmcnt(13)
	v_add_f32_e32 v1, v1, v20
	s_waitcnt vmcnt(12)
	v_add_f32_e32 v1, v1, v21
	s_waitcnt vmcnt(11)
	v_add_f32_e32 v1, v1, v28
	s_waitcnt vmcnt(10)
	v_add_f32_e32 v1, v1, v29
	s_waitcnt vmcnt(9)
	v_add_f32_e32 v1, v1, v30
	s_waitcnt vmcnt(8)
	v_add_f32_e32 v1, v1, v31
	s_waitcnt vmcnt(7)
	v_add_f32_e32 v1, v1, v32
	s_waitcnt vmcnt(6)
	v_add_f32_e32 v1, v1, v33
	v_mul_f32_e32 v12, 0x3a800000, v1
	v_mbcnt_lo_u32_b32 v1, -1, 0
	v_mbcnt_hi_u32_b32 v3, -1, v1
	v_xor_b32_e32 v13, 32, v3
	v_lshlrev_b32_e32 v183, 2, v13
	v_xor_b32_e32 v13, 16, v3
	v_lshlrev_b32_e32 v181, 2, v13
	v_xor_b32_e32 v13, 8, v3
	v_lshlrev_b32_e32 v1, 2, v13
	v_xor_b32_e32 v13, 4, v3
	v_lshlrev_b32_e32 v180, 2, v13
	v_xor_b32_e32 v13, 2, v3
	v_lshlrev_b32_e32 v182, 2, v13
	v_xor_b32_e32 v13, 1, v3
	v_lshlrev_b32_e32 v184, 2, v13
	v_cmp_eq_u32_e32 vcc, 0, v3
	v_mov_b32_e32 v13, v12
	s_waitcnt vmcnt(4)
	v_pk_mul_f32 v[14:15], v[12:13], v[4:5]
	v_pk_mul_f32 v[16:17], v[12:13], v[6:7]
	v_pk_mul_f32 v[18:19], v[12:13], v[8:9]
	v_pk_mul_f32 v[20:21], v[12:13], v[10:11]
	v_add_f32_dpp v14, v14, v14 quad_perm:[1,0,3,2] row_mask:0xf bank_mask:0xf
	v_add_f32_dpp v15, v15, v15 quad_perm:[1,0,3,2] row_mask:0xf bank_mask:0xf
	v_add_f32_dpp v16, v16, v16 quad_perm:[1,0,3,2] row_mask:0xf bank_mask:0xf
	v_add_f32_dpp v17, v17, v17 quad_perm:[1,0,3,2] row_mask:0xf bank_mask:0xf
	v_add_f32_dpp v18, v18, v18 quad_perm:[1,0,3,2] row_mask:0xf bank_mask:0xf
	v_add_f32_dpp v19, v19, v19 quad_perm:[1,0,3,2] row_mask:0xf bank_mask:0xf
	v_add_f32_dpp v20, v20, v20 quad_perm:[1,0,3,2] row_mask:0xf bank_mask:0xf
	v_add_f32_dpp v21, v21, v21 quad_perm:[1,0,3,2] row_mask:0xf bank_mask:0xf
	v_add_f32_dpp v14, v14, v14 quad_perm:[2,3,0,1] row_mask:0xf bank_mask:0xf
	v_add_f32_dpp v15, v15, v15 quad_perm:[2,3,0,1] row_mask:0xf bank_mask:0xf
	v_add_f32_dpp v16, v16, v16 quad_perm:[2,3,0,1] row_mask:0xf bank_mask:0xf
	v_add_f32_dpp v17, v17, v17 quad_perm:[2,3,0,1] row_mask:0xf bank_mask:0xf
	v_add_f32_dpp v18, v18, v18 quad_perm:[2,3,0,1] row_mask:0xf bank_mask:0xf
	v_add_f32_dpp v19, v19, v19 quad_perm:[2,3,0,1] row_mask:0xf bank_mask:0xf
	v_add_f32_dpp v20, v20, v20 quad_perm:[2,3,0,1] row_mask:0xf bank_mask:0xf
	v_add_f32_dpp v21, v21, v21 quad_perm:[2,3,0,1] row_mask:0xf bank_mask:0xf
	v_add_f32_dpp v14, v14, v14 row_half_mirror row_mask:0xf bank_mask:0xf
	v_add_f32_dpp v15, v15, v15 row_half_mirror row_mask:0xf bank_mask:0xf
	v_add_f32_dpp v16, v16, v16 row_half_mirror row_mask:0xf bank_mask:0xf
	v_add_f32_dpp v17, v17, v17 row_half_mirror row_mask:0xf bank_mask:0xf
	v_add_f32_dpp v18, v18, v18 row_half_mirror row_mask:0xf bank_mask:0xf
	v_add_f32_dpp v19, v19, v19 row_half_mirror row_mask:0xf bank_mask:0xf
	v_add_f32_dpp v20, v20, v20 row_half_mirror row_mask:0xf bank_mask:0xf
	v_add_f32_dpp v21, v21, v21 row_half_mirror row_mask:0xf bank_mask:0xf
	v_add_f32_dpp v14, v14, v14 row_mirror row_mask:0xf bank_mask:0xf
	v_add_f32_dpp v15, v15, v15 row_mirror row_mask:0xf bank_mask:0xf
	v_add_f32_dpp v16, v16, v16 row_mirror row_mask:0xf bank_mask:0xf
	v_add_f32_dpp v17, v17, v17 row_mirror row_mask:0xf bank_mask:0xf
	v_add_f32_dpp v18, v18, v18 row_mirror row_mask:0xf bank_mask:0xf
	v_add_f32_dpp v19, v19, v19 row_mirror row_mask:0xf bank_mask:0xf
	v_add_f32_dpp v20, v20, v20 row_mirror row_mask:0xf bank_mask:0xf
	v_add_f32_dpp v21, v21, v21 row_mirror row_mask:0xf bank_mask:0xf
	ds_bpermute_b32 v22, v181, v14
	ds_bpermute_b32 v23, v181, v15
	ds_bpermute_b32 v24, v181, v16
	ds_bpermute_b32 v25, v181, v17
	ds_bpermute_b32 v26, v181, v18
	ds_bpermute_b32 v27, v181, v19
	ds_bpermute_b32 v28, v181, v20
	ds_bpermute_b32 v29, v181, v21
	s_waitcnt lgkmcnt(0)
	v_pk_add_f32 v[14:15], v[14:15], v[22:23]
	v_pk_add_f32 v[16:17], v[16:17], v[24:25]
	v_pk_add_f32 v[18:19], v[18:19], v[26:27]
	v_pk_add_f32 v[20:21], v[20:21], v[28:29]
	ds_bpermute_b32 v22, v183, v14
	ds_bpermute_b32 v23, v183, v15
	ds_bpermute_b32 v24, v183, v16
	ds_bpermute_b32 v25, v183, v17
	ds_bpermute_b32 v26, v183, v18
	ds_bpermute_b32 v27, v183, v19
	ds_bpermute_b32 v28, v183, v20
	ds_bpermute_b32 v29, v183, v21
	s_waitcnt lgkmcnt(0)
	v_pk_add_f32 v[14:15], v[14:15], v[22:23]
	v_pk_add_f32 v[16:17], v[16:17], v[24:25]
	v_pk_add_f32 v[18:19], v[18:19], v[26:27]
	v_pk_add_f32 v[20:21], v[20:21], v[28:29]
	s_and_saveexec_b64 s[4:5], vcc
	s_cbranch_execz .LBB5_2
	v_lshrrev_b32_e32 v22, 1, v0
	v_add_u32_e32 v22, 0x20000, v22
	ds_write_b128 v22, v[14:17]
	ds_write_b128 v22, v[18:21] offset:16

.LBB5_176:
	s_or_b64 exec, exec, s[2:3]
	v_mov_b32_e32 v2, 0
	s_waitcnt lgkmcnt(0)
	s_barrier
	ds_read_b32 v2, v2
	s_waitcnt lgkmcnt(0)
	v_cmp_eq_u32_e32 vcc, 0, v2
	s_cbranch_vccnz .LBB5_184
	s_movk_i32 s2, 0x80
	v_cmp_gt_u32_e32 vcc, s2, v0
	v_lshl_add_u32 v20, v0, 2, 0
	s_and_saveexec_b64 s[2:3], vcc
	s_cbranch_execz .LBB5_180
	s_and_b32 s4, s34, 0xffffffe
	v_or_b32_e32 v3, s4, v187
	v_lshlrev_b32_e32 v4, 4, v3
	v_lshl_add_u32 v2, v187, 2, 0
	v_ashrrev_i32_e32 v5, 31, v4
	v_add_u32_e32 v2, 0x22200, v2
	v_lshl_add_u64 v[4:5], v[4:5], 2, s[22:23]
	ds_read_b32 v2, v2
	global_load_dword v21, v[4:5], off sc1
	global_load_dword v15, v[4:5], off offset:4 sc1
	global_load_dword v32, v[4:5], off offset:8 sc1
	global_load_dword v17, v[4:5], off offset:12 sc1
	global_load_dword v33, v[4:5], off offset:16 sc1
	global_load_dword v19, v[4:5], off offset:20 sc1
	global_load_dword v34, v[4:5], off offset:24 sc1
	global_load_dword v23, v[4:5], off offset:28 sc1
	global_load_dword v35, v[4:5], off offset:32 sc1
	global_load_dword v25, v[4:5], off offset:36 sc1
	global_load_dword v36, v[4:5], off offset:40 sc1
	global_load_dword v27, v[4:5], off offset:44 sc1
	global_load_dword v37, v[4:5], off offset:48 sc1
	global_load_dword v29, v[4:5], off offset:52 sc1
	global_load_dword v38, v[4:5], off offset:56 sc1
	v_and_or_b32 v6, s34, -2, v187
	v_ashrrev_i32_e32 v7, 31, v6
	v_lshlrev_b64 v[6:7], 11, v[6:7]
	v_mov_b32_e32 v11, 0
	v_lshl_add_u64 v[6:7], s[20:21], 0, v[6:7]
	v_lshl_add_u64 v[6:7], v[6:7], 0, v[10:11]
	global_load_dword v31, v[4:5], off offset:60 sc1
	global_load_dword v14, v[6:7], off sc1
	global_load_dword v16, v[6:7], off offset:256 sc1
	global_load_dword v18, v[6:7], off offset:512 sc1
	global_load_dword v22, v[6:7], off offset:768 sc1
	global_load_dword v24, v[6:7], off offset:1024 sc1
	global_load_dword v26, v[6:7], off offset:1280 sc1
	global_load_dword v28, v[6:7], off offset:1536 sc1
	global_load_dword v30, v[6:7], off offset:1792 sc1
	s_waitcnt lgkmcnt(0)
	v_lshl_or_b32 v4, v2, 6, v189
	v_ashrrev_i32_e32 v5, 31, v4
	v_ashrrev_i32_e32 v3, 31, v2
	v_lshl_add_u64 v[4:5], v[4:5], 2, s[36:37]
	v_lshlrev_b64 v[6:7], 11, v[2:3]
	global_load_dword v3, v[4:5], off
	v_mov_b32_e32 v13, v11
	v_lshl_add_u64 v[6:7], s[38:39], 0, v[6:7]
	v_lshl_add_u64 v[12:13], v[6:7], 0, v[12:13]
	global_load_dwordx4 v[4:7], v[12:13], off
	global_load_dwordx4 v[8:11], v[12:13], off offset:16
	v_lshlrev_b32_e32 v208, 5, v2
	global_load_dwordx4 v[200:203], v208, s[10:11]
	global_load_dwordx4 v[204:207], v208, s[10:11] offset:16
	s_mov_b32 s4, 0xff61b1e6
	s_waitcnt vmcnt(26)
	v_max3_f32 v12, v21, s4, v32
	s_waitcnt vmcnt(22)
	v_max3_f32 v12, v12, v33, v34
	s_waitcnt vmcnt(18)
	v_max3_f32 v12, v12, v35, v36
	s_waitcnt vmcnt(14)
	v_max3_f32 v12, v12, v37, v38
	v_sub_f32_e32 v13, v21, v12
	v_sub_f32_e32 v21, v32, v12
	v_sub_f32_e32 v32, v33, v12
	v_sub_f32_e32 v33, v34, v12
	v_sub_f32_e32 v34, v35, v12
	v_sub_f32_e32 v35, v36, v12
	v_sub_f32_e32 v36, v37, v12
	v_sub_f32_e32 v12, v38, v12
	v_mul_f32_e32 v13, 0x3fb8aa3b, v13
	v_mul_f32_e32 v21, 0x3fb8aa3b, v21
	v_mul_f32_e32 v41, 0x3fb8aa3b, v12
	v_exp_f32_e32 v12, v13
	v_mul_f32_e32 v37, 0x3fb8aa3b, v32
	v_exp_f32_e32 v32, v21
	v_mul_f32_e32 v33, 0x3fb8aa3b, v33
	v_mul_f32_e32 v38, 0x3fb8aa3b, v34
	v_exp_f32_e32 v34, v37
	v_mul_f32_e32 v39, 0x3fb8aa3b, v36
	v_exp_f32_e32 v36, v33
	v_mul_f32_e32 v35, 0x3fb8aa3b, v35
	v_exp_f32_e32 v38, v38
	s_waitcnt vmcnt(12)
	v_pk_fma_f32 v[12:13], v[12:13], v[14:15], 0 op_sel_hi:[0,1,0]
	v_exp_f32_e32 v40, v35
	s_waitcnt vmcnt(11)
	v_pk_fma_f32 v[12:13], v[32:33], v[16:17], v[12:13] op_sel_hi:[0,1,1]
	v_exp_f32_e32 v42, v39
	s_waitcnt vmcnt(10)
	v_pk_fma_f32 v[12:13], v[34:35], v[18:19], v[12:13] op_sel_hi:[0,1,1]
	v_exp_f32_e32 v44, v41
	s_waitcnt vmcnt(9)
	v_pk_fma_f32 v[12:13], v[36:37], v[22:23], v[12:13] op_sel_hi:[0,1,1]
	s_waitcnt vmcnt(8)
	v_pk_fma_f32 v[12:13], v[38:39], v[24:25], v[12:13] op_sel_hi:[0,1,1]
	s_waitcnt vmcnt(7)
	v_pk_fma_f32 v[12:13], v[40:41], v[26:27], v[12:13] op_sel_hi:[0,1,1]
	s_waitcnt vmcnt(6)
	v_pk_fma_f32 v[12:13], v[42:43], v[28:29], v[12:13] op_sel_hi:[0,1,1]
	s_waitcnt vmcnt(5)
	v_pk_fma_f32 v[12:13], v[44:45], v[30:31], v[12:13] op_sel_hi:[0,1,1]
	v_div_scale_f32 v14, s[4:5], v13, v13, v12
	v_rcp_f32_e32 v15, v14
	v_div_scale_f32 v16, vcc, v12, v13, v12
	v_fma_f32 v17, -v14, v15, 1.0
	v_fmac_f32_e32 v15, v17, v15
	v_mul_f32_e32 v17, v16, v15
	v_fma_f32 v18, -v14, v17, v16
	v_fmac_f32_e32 v17, v18, v15
	v_fma_f32 v14, -v14, v17, v16
	v_div_fmas_f32 v14, v14, v15, v17
	v_div_fixup_f32 v12, v14, v13, v12
	s_waitcnt vmcnt(4)
	v_add_f32_e32 v3, v12, v3
	v_max_f32_e32 v22, 0, v3
	s_waitcnt vmcnt(3)
	v_pk_mul_f32 v[12:13], v[22:23], v[4:5] op_sel_hi:[0,1]
	ds_bpermute_b32 v12, v183, v12
	ds_bpermute_b32 v13, v183, v13
	v_pk_mul_f32 v[14:15], v[22:23], v[6:7] op_sel_hi:[0,1]
	s_waitcnt vmcnt(2)
	v_pk_mul_f32 v[16:17], v[22:23], v[8:9] op_sel_hi:[0,1]
	ds_bpermute_b32 v14, v183, v14
	ds_bpermute_b32 v15, v183, v15
	s_waitcnt lgkmcnt(2)
	v_pk_fma_f32 v[4:5], v[22:23], v[4:5], v[12:13] op_sel_hi:[0,1,1]
	ds_bpermute_b32 v12, v181, v4
	ds_bpermute_b32 v13, v181, v5
	ds_bpermute_b32 v16, v183, v16
	ds_bpermute_b32 v17, v183, v17
	v_pk_mul_f32 v[18:19], v[22:23], v[10:11] op_sel_hi:[0,1]
	ds_bpermute_b32 v18, v183, v18
	s_waitcnt lgkmcnt(3)
	v_pk_add_f32 v[4:5], v[4:5], v[12:13]
	ds_bpermute_b32 v12, v1, v4
	ds_bpermute_b32 v13, v1, v5
	ds_bpermute_b32 v19, v183, v19
	v_pk_fma_f32 v[6:7], v[22:23], v[6:7], v[14:15] op_sel_hi:[0,1,1]
	s_waitcnt lgkmcnt(4)
	v_pk_fma_f32 v[8:9], v[22:23], v[8:9], v[16:17] op_sel_hi:[0,1,1]
	ds_bpermute_b32 v14, v181, v6
	s_waitcnt lgkmcnt(2)
	v_pk_add_f32 v[4:5], v[4:5], v[12:13]
	ds_bpermute_b32 v15, v181, v7
	ds_bpermute_b32 v12, v180, v4
	ds_bpermute_b32 v13, v180, v5
	ds_bpermute_b32 v16, v181, v8
	ds_bpermute_b32 v17, v181, v9
	s_waitcnt lgkmcnt(6)
	v_pk_fma_f32 v[10:11], v[22:23], v[10:11], v[18:19] op_sel_hi:[0,1,1]
	ds_bpermute_b32 v18, v181, v10
	ds_bpermute_b32 v19, v181, v11
	s_waitcnt lgkmcnt(6)
	v_pk_add_f32 v[6:7], v[6:7], v[14:15]
	s_waitcnt lgkmcnt(4)
	v_pk_add_f32 v[4:5], v[4:5], v[12:13]
	s_waitcnt lgkmcnt(2)
	v_pk_add_f32 v[14:15], v[8:9], v[16:17]
	ds_bpermute_b32 v8, v1, v6
	ds_bpermute_b32 v9, v1, v7
	ds_bpermute_b32 v12, v182, v4
	ds_bpermute_b32 v13, v182, v5
	s_waitcnt lgkmcnt(4)
	v_pk_add_f32 v[10:11], v[10:11], v[18:19]
	ds_bpermute_b32 v16, v1, v14
	s_waitcnt lgkmcnt(3)
	v_pk_add_f32 v[6:7], v[6:7], v[8:9]
	ds_bpermute_b32 v17, v1, v15
	s_waitcnt lgkmcnt(2)
	v_pk_add_f32 v[4:5], v[4:5], v[12:13]
	ds_bpermute_b32 v12, v1, v10
	ds_bpermute_b32 v13, v1, v11
	ds_bpermute_b32 v8, v180, v6
	ds_bpermute_b32 v9, v180, v7
	s_waitcnt lgkmcnt(4)
	v_pk_add_f32 v[14:15], v[14:15], v[16:17]
	ds_bpermute_b32 v16, v180, v14
	s_waitcnt lgkmcnt(3)
	v_pk_add_f32 v[12:13], v[10:11], v[12:13]
	ds_bpermute_b32 v17, v180, v15
	s_waitcnt lgkmcnt(2)
	v_pk_add_f32 v[8:9], v[6:7], v[8:9]
	ds_bpermute_b32 v18, v180, v12
	ds_bpermute_b32 v19, v180, v13
	ds_bpermute_b32 v24, v182, v8
	ds_bpermute_b32 v25, v182, v9
	s_waitcnt lgkmcnt(4)
	v_pk_add_f32 v[14:15], v[14:15], v[16:17]
	ds_bpermute_b32 v16, v182, v14
	s_waitcnt lgkmcnt(3)
	v_pk_add_f32 v[18:19], v[12:13], v[18:19]
	ds_bpermute_b32 v17, v182, v15
	s_waitcnt lgkmcnt(2)
	v_pk_add_f32 v[8:9], v[8:9], v[24:25]
	ds_bpermute_b32 v24, v182, v18
	ds_bpermute_b32 v25, v182, v19
	ds_bpermute_b32 v6, v184, v4
	s_waitcnt lgkmcnt(3)
	v_pk_add_f32 v[12:13], v[14:15], v[16:17]
	ds_bpermute_b32 v7, v184, v5
	ds_bpermute_b32 v10, v184, v8
	s_waitcnt lgkmcnt(3)
	v_pk_add_f32 v[16:17], v[18:19], v[24:25]
	ds_bpermute_b32 v11, v184, v9
	ds_bpermute_b32 v14, v184, v12
	ds_bpermute_b32 v15, v184, v13
	ds_bpermute_b32 v18, v184, v16
	ds_bpermute_b32 v19, v184, v17
	v_cmp_eq_u32_e32 vcc, 0, v189
	ds_write_b32 v20, v22 offset:1024
	s_and_b64 exec, exec, vcc
	s_cbranch_execz .LBB5_180
	v_lshlrev_b32_e32 v2, 3, v2
	v_ashrrev_i32_e32 v3, 31, v2
	v_lshl_add_u64 v[2:3], v[2:3], 2, s[10:11]
	s_waitcnt lgkmcnt(7)
	v_pk_add_f32 v[2:3], v[4:5], v[6:7]
	s_waitcnt lgkmcnt(5)
	v_pk_add_f32 v[4:5], v[8:9], v[10:11]
	v_add_u32_e32 v1, 0, v146
	s_waitcnt lgkmcnt(3)
	v_pk_add_f32 v[6:7], v[12:13], v[14:15]
	s_waitcnt lgkmcnt(1)
	v_pk_add_f32 v[8:9], v[16:17], v[18:19]
	s_waitcnt vmcnt(1)
	v_pk_add_f32 v[2:3], v[2:3], v[200:201]
	v_pk_add_f32 v[4:5], v[4:5], v[202:203]
	s_waitcnt vmcnt(0)
	v_pk_add_f32 v[6:7], v[6:7], v[204:205]
	v_pk_add_f32 v[8:9], v[8:9], v[206:207]
	ds_write_b128 v1, v[2:5] offset:1536
	ds_write_b128 v1, v[6:9] offset:1552
